# v34 + retention chunk-state unit: its 8 K/V tile loads issued together (4 serialized load round trips per unit -> 1)
# baseline (speedup 1.0000x reference)
.LBB0_501:
	s_bfe_u32 s6, s12, 0x20003
	s_lshl_b32 s7, s0, 6
	s_or_b32 s0, s6, s30
	s_lshl_b64 s[16:17], s[0:1], 2
	s_add_u32 s16, s8, s16
	v_readlane_b32 s0, v254, 61
	s_addc_u32 s17, s9, s17
	s_or_b32 s0, s6, s0
	global_load_dword v15, v97, s[16:17]
	s_lshl_b64 s[16:17], s[0:1], 2
	v_mov_b32_e32 v14, 0x7f
	s_add_u32 s16, s8, s16
	v_bitop3_b32 v13, s7, v14, v16 bitop3:0xc8
	s_addc_u32 s17, s9, s17
	v_add_u32_e32 v2, s2, v13
	v_mov_b64_e32 v[0:1], s[4:5]
	v_or_b32_e32 v12, s7, v16
	global_load_dword v20, v97, s[16:17]
	v_mad_i64_i32 v[0:1], s[16:17], v2, s95, v[0:1]
	s_lshl_b32 s0, s6, 8
	v_lshl_add_u64 v[4:5], v[0:1], 0, s[0:1]
	v_ashrrev_i32_e32 v0, 4, v12
	v_and_b32_e32 v18, -8, v0
	s_mov_b64 s[18:19], 0x1000
	v_ashrrev_i32_e32 v19, 31, v18
	v_lshl_add_u64 v[8:9], v[4:5], 0, s[18:19]
	v_lshlrev_b64 v[6:7], 1, v[18:19]
	v_lshl_add_u64 v[0:1], v[8:9], 0, v[6:7]
	s_barrier
	v_mov_b32_e32 v100, v0
	v_mov_b32_e32 v101, v1
	global_load_dwordx4 v[0:3], v[100:101], off
	s_mov_b64 s[20:21], 0x1400
	v_lshl_add_u64 v[10:11], v[4:5], 0, s[20:21]
	v_lshl_add_u64 v[4:5], v[10:11], 0, v[6:7]
	v_mov_b32_e32 v102, v4
	v_mov_b32_e32 v103, v5
	global_load_dwordx4 v[4:7], v[102:103], off
	global_load_dwordx4 v[104:107], v[100:101], off offset:64
	global_load_dwordx4 v[108:111], v[102:103], off offset:64
	global_load_dwordx4 v[112:115], v[100:101], off offset:128
	global_load_dwordx4 v[116:119], v[102:103], off offset:128
	global_load_dwordx4 v[120:123], v[100:101], off offset:192
	global_load_dwordx4 v[124:127], v[102:103], off offset:192
	v_bitop3_b32 v14, s7, v14, v16 bitop3:4
	v_cvt_f32_ubyte0_e32 v17, v14
	v_cvt_f32_ubyte0_e32 v19, v13
	s_movk_i32 s0, 0x88
	s_waitcnt vmcnt(12)
	v_mul_lo_u32 v22, v18, s0
	v_add_lshl_u32 v18, v22, v13, 1
	v_add_u32_e32 v14, 0x88, v13
	s_waitcnt vmcnt(11)
	v_add_u32_e32 v25, 0, v18
	v_add_lshl_u32 v21, v22, v14, 1
	v_add_u32_e32 v18, s3, v18
	v_add_u32_e32 v26, s3, v21
	s_waitcnt vmcnt(10)
	v_add_u32_e32 v28, 0, v21
	v_add_u32_e32 v23, 0x110, v22
	v_add_u32_e32 v27, v23, v13
	v_add_u32_e32 v23, v23, v14
	v_lshl_add_u32 v27, v27, 1, s3
	v_lshl_add_u32 v23, v23, 1, s3
	v_add_u32_e32 v24, 0x220, v22
	v_add_u32_e32 v21, v24, v13
	v_add_u32_e32 v24, v24, v14
	v_lshl_add_u32 v21, v21, 1, s3
	v_lshl_add_u32 v24, v24, 1, s3
	v_bfe_u32 v68, v16, 5, 1
	v_and_b32_e32 v69, 31, v16
	v_bfe_u32 v78, v12, 6, 2
	s_cmp_gt_i32 s13, 1
	s_waitcnt vmcnt(9)
	v_mul_f32_e32 v15, v15, v17
	v_exp_f32_e32 v17, v15
	s_waitcnt vmcnt(8)
	v_mul_f32_e32 v15, v20, v19
	v_exp_f32_e32 v15, v15
	s_waitcnt vmcnt(7)
	v_lshlrev_b32_e32 v19, 16, v0
	v_and_b32_e32 v0, 0xffff0000, v0
	v_mul_f32_e32 v30, v17, v19
	v_mul_f32_e32 v31, v17, v0
	v_cvt_pk_bf16_f32 v30, v30, v30
	v_mul_f32_e32 v19, v15, v19
	v_mul_f32_e32 v0, v15, v0
	v_lshlrev_b32_e32 v20, 16, v1
	ds_write_b16 v25, v30
	v_cvt_pk_bf16_f32 v30, v31, v31
	ds_write_b16 v25, v30 offset:272
	v_cvt_pk_bf16_f32 v19, v19, v19
	ds_write_b16 v25, v19 offset:34816
	v_cvt_pk_bf16_f32 v0, v0, v0
	v_and_b32_e32 v1, 0xffff0000, v1
	v_mul_f32_e32 v32, v17, v20
	s_waitcnt vmcnt(6)
	ds_write_b16 v18, v4
	ds_write_b16 v25, v0 offset:35088
	ds_write_b16_d16_hi v26, v4
	v_cvt_pk_bf16_f32 v0, v32, v32
	v_mul_f32_e32 v33, v17, v1
	ds_write_b16 v25, v0 offset:544
	v_cvt_pk_bf16_f32 v0, v33, v33
	v_mul_f32_e32 v20, v15, v20
	ds_write_b16 v28, v0 offset:544
	v_cvt_pk_bf16_f32 v0, v20, v20
	v_lshlrev_b32_e32 v29, 16, v2
	v_mul_f32_e32 v1, v15, v1
	ds_write_b16 v25, v0 offset:35360
	v_cvt_pk_bf16_f32 v0, v1, v1
	v_and_b32_e32 v2, 0xffff0000, v2
	v_mul_f32_e32 v34, v17, v29
	ds_write_b16 v28, v0 offset:35360
	ds_write_b16 v27, v5
	ds_write_b16_d16_hi v23, v5
	v_cvt_pk_bf16_f32 v0, v34, v34
	v_mul_f32_e32 v35, v17, v2
	ds_write_b16 v25, v0 offset:1088
	v_cvt_pk_bf16_f32 v0, v35, v35
	v_mul_f32_e32 v29, v15, v29
	ds_write_b16 v28, v0 offset:1088
	v_cvt_pk_bf16_f32 v0, v29, v29
	v_mul_f32_e32 v2, v15, v2
	ds_write_b16 v25, v0 offset:35904
	v_cvt_pk_bf16_f32 v0, v2, v2
	ds_write_b16 v28, v0 offset:35904
	ds_write_b16 v21, v6
	ds_write_b16_d16_hi v24, v6
	v_lshlrev_b32_e32 v0, 16, v3
	v_mul_f32_e32 v2, v17, v0
	v_and_b32_e32 v1, 0xffff0000, v3
	v_cvt_pk_bf16_f32 v2, v2, v2
	ds_write_b16 v25, v2 offset:1632
	v_mul_f32_e32 v2, v17, v1
	v_mul_f32_e32 v0, v15, v0
	v_cvt_pk_bf16_f32 v2, v2, v2
	ds_write_b16 v28, v2 offset:1632
	v_cvt_pk_bf16_f32 v0, v0, v0
	ds_write_b16 v25, v0 offset:36448
	v_mul_f32_e32 v0, v15, v1
	v_cvt_pk_bf16_f32 v6, v0, v0
	v_add_u32_e32 v0, 0x200, v12
	v_ashrrev_i32_e32 v0, 4, v0
	v_and_b32_e32 v0, -8, v0
	v_ashrrev_i32_e32 v1, 31, v0
	v_lshlrev_b64 v[2:3], 1, v[0:1]
	v_lshl_add_u64 v[4:5], v[8:9], 0, v[2:3]
	s_waitcnt vmcnt(4)
	v_mov_b32_e32 v18, v104
	v_mov_b32_e32 v19, v105
	v_mov_b32_e32 v20, v106
	v_mov_b32_e32 v21, v107
	v_lshl_add_u64 v[2:3], v[10:11], 0, v[2:3]
	v_mov_b32_e32 v2, v108
	v_mov_b32_e32 v3, v109
	v_mov_b32_e32 v4, v110
	v_mov_b32_e32 v5, v111
	v_add_u32_e32 v1, 0x330, v22
	v_mul_lo_u32 v22, v0, s0
	v_add_u32_e32 v0, v1, v13
	v_add_u32_e32 v1, v1, v14
	v_lshl_add_u32 v0, v0, 1, s3
	v_lshl_add_u32 v1, v1, 1, s3
	ds_write_b16 v28, v6 offset:36448
	ds_write_b16 v0, v7
	ds_write_b16_d16_hi v1, v7
	v_add_lshl_u32 v23, v22, v13, 1
	v_add_u32_e32 v27, 0, v23
	v_add_lshl_u32 v24, v22, v14, 1
	v_add_u32_e32 v23, s3, v23
	v_add_u32_e32 v29, s3, v24
	v_add_u32_e32 v24, 0, v24
	v_add_u32_e32 v25, 0x110, v22
	v_add_u32_e32 v30, v25, v13
	v_add_u32_e32 v25, v25, v14
	v_lshl_add_u32 v30, v30, 1, s3
	v_lshl_add_u32 v25, v25, 1, s3
	v_add_u32_e32 v26, 0x220, v22
	v_add_u32_e32 v31, v26, v13
	v_add_u32_e32 v26, v26, v14
	v_lshl_add_u32 v31, v31, 1, s3
	v_lshl_add_u32 v26, v26, 1, s3
	s_waitcnt vmcnt(1)
	v_lshlrev_b32_e32 v0, 16, v18
	v_mul_f32_e32 v28, v17, v0
	v_and_b32_e32 v1, 0xffff0000, v18
	v_mul_f32_e32 v0, v15, v0
	v_cvt_pk_bf16_f32 v28, v28, v28
	v_mul_f32_e32 v32, v17, v1
	ds_write_b16 v27, v28
	v_cvt_pk_bf16_f32 v28, v32, v32
	ds_write_b16 v27, v28 offset:272
	v_cvt_pk_bf16_f32 v0, v0, v0
	v_lshlrev_b32_e32 v6, 16, v19
	v_mul_f32_e32 v1, v15, v1
	ds_write_b16 v27, v0 offset:34816
	v_cvt_pk_bf16_f32 v0, v1, v1
	v_and_b32_e32 v7, 0xffff0000, v19
	v_mul_f32_e32 v33, v17, v6
	s_waitcnt vmcnt(0)
	ds_write_b16 v23, v2
	ds_write_b16 v27, v0 offset:35088
	ds_write_b16_d16_hi v29, v2
	v_cvt_pk_bf16_f32 v0, v33, v33
	v_mul_f32_e32 v34, v17, v7
	ds_write_b16 v27, v0 offset:544
	v_cvt_pk_bf16_f32 v0, v34, v34
	v_mul_f32_e32 v6, v15, v6
	ds_write_b16 v24, v0 offset:544
	v_cvt_pk_bf16_f32 v0, v6, v6
	v_lshlrev_b32_e32 v18, 16, v20
	v_mul_f32_e32 v7, v15, v7
	ds_write_b16 v27, v0 offset:35360
	v_cvt_pk_bf16_f32 v0, v7, v7
	v_and_b32_e32 v19, 0xffff0000, v20
	v_mul_f32_e32 v35, v17, v18
	ds_write_b16 v24, v0 offset:35360
	ds_write_b16 v30, v3
	ds_write_b16_d16_hi v25, v3
	v_cvt_pk_bf16_f32 v0, v35, v35
	v_mul_f32_e32 v36, v17, v19
	ds_write_b16 v27, v0 offset:1088
	v_cvt_pk_bf16_f32 v0, v36, v36
	v_mul_f32_e32 v18, v15, v18
	ds_write_b16 v24, v0 offset:1088
	v_cvt_pk_bf16_f32 v0, v18, v18
	v_lshlrev_b32_e32 v20, 16, v21
	v_mul_f32_e32 v19, v15, v19
	ds_write_b16 v27, v0 offset:35904
	v_cvt_pk_bf16_f32 v0, v19, v19
	ds_write_b16 v24, v0 offset:35904
	ds_write_b16 v31, v4
	ds_write_b16_d16_hi v26, v4
	v_mul_f32_e32 v0, v17, v20
	v_and_b32_e32 v21, 0xffff0000, v21
	v_cvt_pk_bf16_f32 v0, v0, v0
	ds_write_b16 v27, v0 offset:1632
	v_mul_f32_e32 v0, v17, v21
	v_cvt_pk_bf16_f32 v0, v0, v0
	ds_write_b16 v24, v0 offset:1632
	v_mul_f32_e32 v0, v15, v20
	v_cvt_pk_bf16_f32 v0, v0, v0
	ds_write_b16 v27, v0 offset:36448
	v_mul_f32_e32 v0, v15, v21
	v_cvt_pk_bf16_f32 v4, v0, v0
	v_add_u32_e32 v0, 0x400, v12
	v_ashrrev_i32_e32 v0, 4, v0
	v_and_b32_e32 v6, -8, v0
	v_ashrrev_i32_e32 v7, 31, v6
	v_lshlrev_b64 v[0:1], 1, v[6:7]
	v_lshl_add_u64 v[2:3], v[8:9], 0, v[0:1]
	s_waitcnt vmcnt(2)
	v_mov_b32_e32 v18, v112
	v_mov_b32_e32 v19, v113
	v_mov_b32_e32 v20, v114
	v_mov_b32_e32 v21, v115
	v_lshl_add_u64 v[0:1], v[10:11], 0, v[0:1]
	v_mov_b32_e32 v0, v116
	v_mov_b32_e32 v1, v117
	v_mov_b32_e32 v2, v118
	v_mov_b32_e32 v3, v119
	v_mul_lo_u32 v23, v6, s0
	v_add_u32_e32 v6, 0x330, v22
	v_add_u32_e32 v27, v6, v13
	v_add_u32_e32 v6, v6, v14
	v_lshl_add_u32 v27, v27, 1, s3
	v_lshl_add_u32 v6, v6, 1, s3
	ds_write_b16 v24, v4 offset:36448
	ds_write_b16 v27, v5
	ds_write_b16_d16_hi v6, v5
	v_add_lshl_u32 v7, v23, v13, 1
	v_add_u32_e32 v28, 0, v7
	v_add_lshl_u32 v22, v23, v14, 1
	v_add_u32_e32 v7, s3, v7
	v_add_u32_e32 v29, s3, v22
	v_add_u32_e32 v22, 0, v22
	v_add_u32_e32 v25, 0x110, v23
	v_add_u32_e32 v30, v25, v13
	v_add_u32_e32 v25, v25, v14
	v_lshl_add_u32 v30, v30, 1, s3
	v_lshl_add_u32 v25, v25, 1, s3
	v_add_u32_e32 v26, 0x220, v23
	v_add_u32_e32 v31, v26, v13
	v_add_u32_e32 v26, v26, v14
	v_lshl_add_u32 v31, v31, 1, s3
	v_lshl_add_u32 v26, v26, 1, s3
	s_waitcnt vmcnt(1)
	v_lshlrev_b32_e32 v4, 16, v18
	v_mul_f32_e32 v27, v17, v4
	v_and_b32_e32 v5, 0xffff0000, v18
	v_mul_f32_e32 v4, v15, v4
	v_cvt_pk_bf16_f32 v27, v27, v27
	v_lshlrev_b32_e32 v6, 16, v19
	v_mul_f32_e32 v32, v17, v5
	ds_write_b16 v28, v27
	v_cvt_pk_bf16_f32 v27, v32, v32
	ds_write_b16 v28, v27 offset:272
	v_cvt_pk_bf16_f32 v4, v4, v4
	v_and_b32_e32 v18, 0xffff0000, v19
	v_mul_f32_e32 v5, v15, v5
	v_mul_f32_e32 v33, v17, v6
	ds_write_b16 v28, v4 offset:34816
	v_cvt_pk_bf16_f32 v4, v5, v5
	s_waitcnt vmcnt(0)
	ds_write_b16 v7, v0
	ds_write_b16 v28, v4 offset:35088
	ds_write_b16_d16_hi v29, v0
	v_cvt_pk_bf16_f32 v0, v33, v33
	v_mul_f32_e32 v34, v17, v18
	ds_write_b16 v28, v0 offset:544
	v_cvt_pk_bf16_f32 v0, v34, v34
	v_mul_f32_e32 v6, v15, v6
	ds_write_b16 v22, v0 offset:544
	v_cvt_pk_bf16_f32 v0, v6, v6
	v_lshlrev_b32_e32 v19, 16, v20
	v_mul_f32_e32 v18, v15, v18
	ds_write_b16 v28, v0 offset:35360
	v_cvt_pk_bf16_f32 v0, v18, v18
	v_and_b32_e32 v20, 0xffff0000, v20
	v_mul_f32_e32 v35, v17, v19
	ds_write_b16 v22, v0 offset:35360
	ds_write_b16 v30, v1
	ds_write_b16_d16_hi v25, v1
	v_cvt_pk_bf16_f32 v0, v35, v35
	v_mul_f32_e32 v36, v17, v20
	ds_write_b16 v28, v0 offset:1088
	v_cvt_pk_bf16_f32 v0, v36, v36
	v_mul_f32_e32 v19, v15, v19
	ds_write_b16 v22, v0 offset:1088
	v_cvt_pk_bf16_f32 v0, v19, v19
	v_lshlrev_b32_e32 v24, 16, v21
	v_mul_f32_e32 v20, v15, v20
	ds_write_b16 v28, v0 offset:35904
	v_cvt_pk_bf16_f32 v0, v20, v20
	v_and_b32_e32 v21, 0xffff0000, v21
	v_mul_f32_e32 v37, v17, v24
	ds_write_b16 v22, v0 offset:35904
	ds_write_b16 v31, v2
	ds_write_b16_d16_hi v26, v2
	v_cvt_pk_bf16_f32 v0, v37, v37
	ds_write_b16 v28, v0 offset:1632
	v_mul_f32_e32 v0, v17, v21
	v_cvt_pk_bf16_f32 v0, v0, v0
	ds_write_b16 v22, v0 offset:1632
	v_mul_f32_e32 v0, v15, v24
	v_cvt_pk_bf16_f32 v0, v0, v0
	ds_write_b16 v28, v0 offset:36448
	v_mul_f32_e32 v0, v15, v21
	v_cvt_pk_bf16_f32 v2, v0, v0
	v_add_u32_e32 v0, 0x600, v12
	v_ashrrev_i32_e32 v0, 4, v0
	v_and_b32_e32 v0, -8, v0
	v_ashrrev_i32_e32 v1, 31, v0
	v_lshlrev_b64 v[4:5], 1, v[0:1]
	v_lshl_add_u64 v[6:7], v[8:9], 0, v[4:5]
	s_waitcnt vmcnt(0)
	v_mov_b32_e32 v18, v120
	v_mov_b32_e32 v19, v121
	v_mov_b32_e32 v20, v122
	v_mov_b32_e32 v21, v123
	v_lshl_add_u64 v[4:5], v[10:11], 0, v[4:5]
	v_mov_b32_e32 v4, v124
	v_mov_b32_e32 v5, v125
	v_mov_b32_e32 v6, v126
	v_mov_b32_e32 v7, v127
	v_add_u32_e32 v1, 0x330, v23
	v_add_u32_e32 v16, v1, v13
	v_add_u32_e32 v1, v1, v14
	v_lshl_add_u32 v1, v1, 1, s3
	v_mul_lo_u32 v0, v0, s0
	v_lshl_add_u32 v16, v16, 1, s3
	ds_write_b16 v22, v2 offset:36448
	ds_write_b16 v16, v3
	ds_write_b16_d16_hi v1, v3
	v_add_lshl_u32 v8, v0, v13, 1
	v_add_u32_e32 v23, 0, v8
	v_add_lshl_u32 v9, v0, v14, 1
	v_add_u32_e32 v8, s3, v8
	v_add_u32_e32 v24, s3, v9
	v_add_u32_e32 v9, 0, v9
	v_add_u32_e32 v10, 0x110, v0
	v_add_u32_e32 v25, v10, v13
	v_add_u32_e32 v10, v10, v14
	v_lshl_add_u32 v25, v25, 1, s3
	v_lshl_add_u32 v10, v10, 1, s3
	v_add_u32_e32 v11, 0x220, v0
	v_add_u32_e32 v26, v11, v13
	v_add_u32_e32 v11, v11, v14
	v_lshl_add_u32 v26, v26, 1, s3
	v_lshl_add_u32 v11, v11, 1, s3
	v_add_u32_e32 v0, 0x330, v0
	s_cselect_b32 s0, 19, 1
	s_lshl_b32 s2, s14, 3
	s_lshl_b32 s6, s6, 1
	s_or_b32 s2, s6, s2
	s_mul_i32 s2, s2, 18
	s_add_i32 s6, s2, s13
	s_ashr_i32 s7, s6, 31
	s_lshl_b64 s[6:7], s[6:7], 16
	s_add_u32 s6, s10, s6
	s_addc_u32 s7, s11, s7
	s_sub_i32 s0, s0, s13
	s_add_i32 s0, s0, s2
	s_add_i32 s0, s0, 18
	s_lshl_b64 s[14:15], s[0:1], 16
	s_add_u32 s14, s10, s14
	s_addc_u32 s15, s11, s15
	s_movk_i32 s0, 0x2000
	s_add_i32 s12, s12, s80
	s_cmpk_lt_i32 s12, 0x240
	s_waitcnt vmcnt(1)
	v_lshlrev_b32_e32 v1, 16, v18
	v_mul_f32_e32 v22, v17, v1
	v_and_b32_e32 v2, 0xffff0000, v18
	v_mul_f32_e32 v1, v15, v1
	v_cvt_pk_bf16_f32 v22, v22, v22
	v_mul_f32_e32 v27, v17, v2
	ds_write_b16 v23, v22
	v_cvt_pk_bf16_f32 v22, v27, v27
	ds_write_b16 v23, v22 offset:272
	v_cvt_pk_bf16_f32 v1, v1, v1
	v_lshlrev_b32_e32 v3, 16, v19
	v_mul_f32_e32 v2, v15, v2
	ds_write_b16 v23, v1 offset:34816
	v_cvt_pk_bf16_f32 v1, v2, v2
	v_and_b32_e32 v16, 0xffff0000, v19
	v_mul_f32_e32 v28, v17, v3
	s_waitcnt vmcnt(0)
	ds_write_b16 v8, v4
	ds_write_b16 v23, v1 offset:35088
	ds_write_b16_d16_hi v24, v4
	v_cvt_pk_bf16_f32 v1, v28, v28
	v_mul_f32_e32 v29, v17, v16
	ds_write_b16 v23, v1 offset:544
	v_cvt_pk_bf16_f32 v1, v29, v29
	v_mul_f32_e32 v3, v15, v3
	ds_write_b16 v9, v1 offset:544
	v_cvt_pk_bf16_f32 v1, v3, v3
	v_lshlrev_b32_e32 v18, 16, v20
	v_mul_f32_e32 v16, v15, v16
	ds_write_b16 v23, v1 offset:35360
	v_cvt_pk_bf16_f32 v1, v16, v16
	v_and_b32_e32 v19, 0xffff0000, v20
	v_mul_f32_e32 v30, v17, v18
	ds_write_b16 v9, v1 offset:35360
	ds_write_b16 v25, v5
	ds_write_b16_d16_hi v10, v5
	v_cvt_pk_bf16_f32 v1, v30, v30
	v_mul_f32_e32 v31, v17, v19
	ds_write_b16 v23, v1 offset:1088
	v_cvt_pk_bf16_f32 v1, v31, v31
	v_mul_f32_e32 v18, v15, v18
	ds_write_b16 v9, v1 offset:1088
	v_cvt_pk_bf16_f32 v1, v18, v18
	v_lshlrev_b32_e32 v20, 16, v21
	v_mul_f32_e32 v19, v15, v19
	ds_write_b16 v23, v1 offset:35904
	v_cvt_pk_bf16_f32 v1, v19, v19
	v_and_b32_e32 v21, 0xffff0000, v21
	v_mul_f32_e32 v32, v17, v20
	ds_write_b16 v9, v1 offset:35904
	ds_write_b16 v26, v6
	ds_write_b16_d16_hi v11, v6
	v_cvt_pk_bf16_f32 v1, v32, v32
	ds_write_b16 v23, v1 offset:1632
	v_mul_f32_e32 v1, v17, v21
	v_cvt_pk_bf16_f32 v1, v1, v1
	ds_write_b16 v9, v1 offset:1632
	v_mul_f32_e32 v1, v15, v20
	v_cvt_pk_bf16_f32 v1, v1, v1
	v_add_u32_e32 v2, v0, v13
	v_add_u32_e32 v0, v0, v14
	ds_write_b16 v23, v1 offset:36448
	v_mul_f32_e32 v1, v15, v21
	v_cvt_pk_bf16_f32 v1, v1, v1
	v_lshl_add_u32 v0, v0, 1, s3
	ds_write_b16 v9, v1 offset:36448
	v_lshl_add_u32 v1, v2, 1, s3
	ds_write_b16_d16_hi v0, v7
	v_lshl_or_b32 v0, v78, 5, v69
	ds_write_b16 v1, v7
	v_mul_u32_u24_e32 v0, 0x110, v0
	v_lshlrev_b32_e32 v1, 4, v68
	v_add3_u32 v79, s3, v0, v1
	s_waitcnt lgkmcnt(0)
	s_barrier
	v_ashrrev_i32_e32 v0, 2, v12
	ds_read_b128 v[16:19], v79
	v_and_b32_e32 v80, 0xffffffc0, v0
	v_add_u32_e32 v4, 0, v1
	v_or_b32_e32 v5, v80, v69
	v_mad_u64_u32 v[66:67], s[16:17], v5, s65, v[4:5]
	ds_read_b128 v[0:3], v66
	s_waitcnt lgkmcnt(0)
	v_mfma_f32_32x32x16_bf16 v[48:63], v[16:19], v[0:3], 0
	ds_read_b128 v[0:3], v66 offset:34816
	s_waitcnt lgkmcnt(0)
	v_mfma_f32_32x32x16_bf16 v[32:47], v[16:19], v[0:3], 0
	v_or_b32_e32 v0, 32, v5
	v_mad_u64_u32 v[64:65], s[16:17], v0, s65, v[4:5]
	ds_read_b128 v[0:3], v64
	ds_read_b128 v[20:23], v64 offset:34816
	ds_read_b128 v[70:73], v79 offset:32
	ds_read_b128 v[74:77], v66 offset:32
	s_waitcnt lgkmcnt(0)
	v_mfma_f32_32x32x16_bf16 v[48:63], v[70:73], v[74:77], v[48:63]
	ds_read_b128 v[74:77], v66 offset:34848
	v_mfma_f32_32x32x16_bf16 v[0:15], v[16:19], v[0:3], 0
	s_waitcnt lgkmcnt(0)
	v_mfma_f32_32x32x16_bf16 v[32:47], v[70:73], v[74:77], v[32:47]
	ds_read_b128 v[74:77], v64 offset:32
	v_mfma_f32_32x32x16_bf16 v[16:31], v[16:19], v[20:23], 0
	s_waitcnt lgkmcnt(0)
	v_mfma_f32_32x32x16_bf16 v[0:15], v[70:73], v[74:77], v[0:15]
	ds_read_b128 v[74:77], v64 offset:34848
	s_waitcnt lgkmcnt(0)
	v_mfma_f32_32x32x16_bf16 v[16:31], v[70:73], v[74:77], v[16:31]
	ds_read_b128 v[70:73], v79 offset:64
	ds_read_b128 v[74:77], v66 offset:64
	s_waitcnt lgkmcnt(0)
	v_mfma_f32_32x32x16_bf16 v[48:63], v[70:73], v[74:77], v[48:63]
	ds_read_b128 v[74:77], v66 offset:34880
	s_waitcnt lgkmcnt(0)
	v_mfma_f32_32x32x16_bf16 v[32:47], v[70:73], v[74:77], v[32:47]
	ds_read_b128 v[74:77], v64 offset:64
	s_waitcnt lgkmcnt(0)
	v_mfma_f32_32x32x16_bf16 v[0:15], v[70:73], v[74:77], v[0:15]
	ds_read_b128 v[74:77], v64 offset:34880
	s_waitcnt lgkmcnt(0)
	v_mfma_f32_32x32x16_bf16 v[16:31], v[70:73], v[74:77], v[16:31]
	ds_read_b128 v[70:73], v79 offset:96
	ds_read_b128 v[74:77], v66 offset:96
	s_waitcnt lgkmcnt(0)
	v_mfma_f32_32x32x16_bf16 v[48:63], v[70:73], v[74:77], v[48:63]
	ds_read_b128 v[74:77], v66 offset:34912
	s_waitcnt lgkmcnt(0)
	v_mfma_f32_32x32x16_bf16 v[32:47], v[70:73], v[74:77], v[32:47]
	ds_read_b128 v[74:77], v64 offset:96
	s_waitcnt lgkmcnt(0)
	v_mfma_f32_32x32x16_bf16 v[0:15], v[70:73], v[74:77], v[0:15]
	ds_read_b128 v[74:77], v64 offset:34912
	s_waitcnt lgkmcnt(0)
	v_mfma_f32_32x32x16_bf16 v[16:31], v[70:73], v[74:77], v[16:31]
	ds_read_b128 v[70:73], v79 offset:128
	ds_read_b128 v[74:77], v66 offset:128
	s_waitcnt lgkmcnt(0)
	v_mfma_f32_32x32x16_bf16 v[48:63], v[70:73], v[74:77], v[48:63]
	ds_read_b128 v[74:77], v66 offset:34944
	s_waitcnt lgkmcnt(0)
	v_mfma_f32_32x32x16_bf16 v[32:47], v[70:73], v[74:77], v[32:47]
	ds_read_b128 v[74:77], v64 offset:128
	s_waitcnt lgkmcnt(0)
	v_mfma_f32_32x32x16_bf16 v[0:15], v[70:73], v[74:77], v[0:15]
	ds_read_b128 v[74:77], v64 offset:34944
	s_waitcnt lgkmcnt(0)
	v_mfma_f32_32x32x16_bf16 v[16:31], v[70:73], v[74:77], v[16:31]
	ds_read_b128 v[70:73], v79 offset:160
	ds_read_b128 v[74:77], v66 offset:160
	s_waitcnt lgkmcnt(0)
	v_mfma_f32_32x32x16_bf16 v[48:63], v[70:73], v[74:77], v[48:63]
	ds_read_b128 v[74:77], v66 offset:34976
	s_waitcnt lgkmcnt(0)
	v_mfma_f32_32x32x16_bf16 v[32:47], v[70:73], v[74:77], v[32:47]
	ds_read_b128 v[74:77], v64 offset:160
	s_waitcnt lgkmcnt(0)
	v_mfma_f32_32x32x16_bf16 v[0:15], v[70:73], v[74:77], v[0:15]
	ds_read_b128 v[74:77], v64 offset:34976
	s_waitcnt lgkmcnt(0)
	v_mfma_f32_32x32x16_bf16 v[16:31], v[70:73], v[74:77], v[16:31]
	ds_read_b128 v[70:73], v79 offset:192
	ds_read_b128 v[74:77], v66 offset:192
	s_waitcnt lgkmcnt(0)
	v_mfma_f32_32x32x16_bf16 v[48:63], v[70:73], v[74:77], v[48:63]
	ds_read_b128 v[74:77], v66 offset:35008
	s_waitcnt lgkmcnt(0)
	v_mfma_f32_32x32x16_bf16 v[32:47], v[70:73], v[74:77], v[32:47]
	ds_read_b128 v[74:77], v64 offset:192
	s_waitcnt lgkmcnt(0)
	v_mfma_f32_32x32x16_bf16 v[0:15], v[70:73], v[74:77], v[0:15]
	ds_read_b128 v[74:77], v64 offset:35008
	s_waitcnt lgkmcnt(0)
	v_mfma_f32_32x32x16_bf16 v[16:31], v[70:73], v[74:77], v[16:31]
	ds_read_b128 v[70:73], v79 offset:224
	ds_read_b128 v[74:77], v66 offset:224
	s_waitcnt lgkmcnt(0)
	v_mfma_f32_32x32x16_bf16 v[48:63], v[70:73], v[74:77], v[48:63]
	ds_read_b128 v[74:77], v66 offset:35040
	s_waitcnt lgkmcnt(0)
	v_mfma_f32_32x32x16_bf16 v[32:47], v[70:73], v[74:77], v[32:47]
	ds_read_b128 v[74:77], v64 offset:224
	ds_read_b128 v[64:67], v64 offset:35040
	s_waitcnt lgkmcnt(0)
	v_mfma_f32_32x32x16_bf16 v[16:31], v[70:73], v[64:67], v[16:31]
	v_lshlrev_b32_e32 v64, 12, v78
	v_lshlrev_b32_e32 v65, 9, v68
	v_or3_b32 v64, v64, v65, v69
	v_add_u32_e32 v64, v64, v80
	v_ashrrev_i32_e32 v65, 31, v64
	v_lshlrev_b64 v[64:65], 2, v[64:65]
	v_lshl_add_u64 v[66:67], s[6:7], 0, v[64:65]
	v_lshl_add_u64 v[64:65], s[14:15], 0, v[64:65]
	global_store_dword v[66:67], v48, off
	global_store_dword v[64:65], v32, off
	global_store_dword v[66:67], v49, off offset:512
	global_store_dword v[64:65], v33, off offset:512
	global_store_dword v[66:67], v50, off offset:1024
	global_store_dword v[64:65], v34, off offset:1024
	global_store_dword v[66:67], v51, off offset:1536
	global_store_dword v[64:65], v35, off offset:1536
	v_add_co_u32_e32 v34, vcc, s63, v66
	s_mov_b64 s[6:7], 0x1200
	s_nop 0
	v_addc_co_u32_e32 v35, vcc, 0, v67, vcc
	v_add_co_u32_e32 v48, vcc, s0, v66
	v_mfma_f32_32x32x16_bf16 v[0:15], v[70:73], v[74:77], v[0:15]
	s_nop 0
	v_addc_co_u32_e32 v49, vcc, 0, v67, vcc
	global_store_dword v[48:49], v52, off offset:-4096
	v_add_co_u32_e32 v68, vcc, s63, v64
	v_lshl_add_u64 v[72:73], v[66:67], 0, s[6:7]
	global_store_dword v[34:35], v53, off offset:512
	v_lshl_add_u64 v[52:53], v[64:65], 0, s[6:7]
	s_mov_b64 s[6:7], 0x1600
	v_addc_co_u32_e32 v69, vcc, 0, v65, vcc
	global_store_dword v[34:35], v54, off offset:1024
	v_lshl_add_u64 v[76:77], v[66:67], 0, s[6:7]
	global_store_dword v[34:35], v55, off offset:1536
	v_lshl_add_u64 v[34:35], v[64:65], 0, s[6:7]
	s_mov_b64 s[6:7], 0x2000
	v_add_co_u32_e32 v70, vcc, s0, v64
	global_store_dword v[68:69], v38, off offset:1024
	global_store_dword v[68:69], v39, off offset:1536
	v_lshl_add_u64 v[38:39], v[66:67], 0, s[6:7]
	v_lshl_add_u64 v[54:55], v[64:65], 0, s[6:7]
	s_mov_b64 s[6:7], 0x2200
	v_addc_co_u32_e32 v71, vcc, 0, v65, vcc
	global_store_dword v[68:69], v37, off offset:512
	global_store_dword v[48:49], v56, off
	v_lshl_add_u64 v[68:69], v[66:67], 0, s[6:7]
	global_store_dword v[48:49], v57, off offset:512
	v_lshl_add_u64 v[56:57], v[64:65], 0, s[6:7]
	s_mov_b64 s[6:7], 0x2400
	global_store_dword v[70:71], v40, off
	global_store_dword v[70:71], v41, off offset:512
	v_lshl_add_u64 v[40:41], v[66:67], 0, s[6:7]
	global_store_dword v[48:49], v58, off offset:1024
	v_lshl_add_u64 v[78:79], v[64:65], 0, s[6:7]
	s_mov_b64 s[6:7], 0x2600
	v_add_co_u32_e32 v58, vcc, s95, v66
	v_lshl_add_u64 v[80:81], v[66:67], 0, s[6:7]
	global_store_dword v[48:49], v59, off offset:1536
	v_lshl_add_u64 v[48:49], v[64:65], 0, s[6:7]
	s_mov_b64 s[6:7], 0x3000
	v_addc_co_u32_e32 v59, vcc, 0, v67, vcc
	global_store_dword v[70:71], v36, off offset:-4096
	global_store_dword v[70:71], v42, off offset:1024
	global_store_dword v[70:71], v43, off offset:1536
	v_lshl_add_u64 v[42:43], v[66:67], 0, s[6:7]
	v_lshl_add_u64 v[70:71], v[64:65], 0, s[6:7]
	v_add_co_u32_e32 v82, vcc, s95, v64
	s_mov_b64 s[6:7], 0x3200
	global_store_dword v[58:59], v60, off
	v_addc_co_u32_e32 v83, vcc, 0, v65, vcc
	v_lshl_add_u64 v[84:85], v[66:67], 0, s[6:7]
	global_store_dword v[58:59], v61, off offset:512
	v_lshl_add_u64 v[60:61], v[64:65], 0, s[6:7]
	s_mov_b64 s[6:7], 0x3400
	global_store_dword v[82:83], v44, off
	global_store_dword v[82:83], v45, off offset:512
	v_lshl_add_u64 v[44:45], v[66:67], 0, s[6:7]
	v_lshl_add_u64 v[86:87], v[64:65], 0, s[6:7]
	s_mov_b64 s[6:7], 0x3600
	v_lshl_add_u64 v[32:33], v[66:67], 0, s[18:19]
	v_lshl_add_u64 v[50:51], v[64:65], 0, s[18:19]
	v_lshl_add_u64 v[36:37], v[66:67], 0, s[20:21]
	v_lshl_add_u64 v[74:75], v[64:65], 0, s[20:21]
	global_store_dword v[58:59], v62, off offset:1024
	global_store_dword v[82:83], v46, off offset:1024
	v_lshl_add_u64 v[88:89], v[66:67], 0, s[6:7]
	global_store_dword v[58:59], v63, off offset:1536
	v_lshl_add_u64 v[58:59], v[64:65], 0, s[6:7]
	global_store_dword v[82:83], v47, off offset:1536
	global_store_dword v[66:67], v0, off offset:128
	global_store_dword v[64:65], v16, off offset:128
	global_store_dword v[66:67], v1, off offset:640
	global_store_dword v[64:65], v17, off offset:640
	global_store_dword v[66:67], v2, off offset:1152
	global_store_dword v[64:65], v18, off offset:1152
	global_store_dword v[66:67], v3, off offset:1664
	global_store_dword v[64:65], v19, off offset:1664
	global_store_dword v[32:33], v4, off offset:128
	global_store_dword v[50:51], v20, off offset:128
	global_store_dword v[72:73], v5, off offset:128
	global_store_dword v[52:53], v21, off offset:128
	global_store_dword v[36:37], v6, off offset:128
	global_store_dword v[74:75], v22, off offset:128
	global_store_dword v[76:77], v7, off offset:128
	global_store_dword v[34:35], v23, off offset:128
	global_store_dword v[38:39], v8, off offset:128
	global_store_dword v[54:55], v24, off offset:128
	global_store_dword v[68:69], v9, off offset:128
	global_store_dword v[56:57], v25, off offset:128
	global_store_dword v[40:41], v10, off offset:128
	global_store_dword v[78:79], v26, off offset:128
	global_store_dword v[80:81], v11, off offset:128
	global_store_dword v[48:49], v27, off offset:128
	global_store_dword v[42:43], v12, off offset:128
	global_store_dword v[70:71], v28, off offset:128
	global_store_dword v[84:85], v13, off offset:128
	global_store_dword v[60:61], v29, off offset:128
	global_store_dword v[44:45], v14, off offset:128
	global_store_dword v[86:87], v30, off offset:128
	global_store_dword v[88:89], v15, off offset:128
	global_store_dword v[58:59], v31, off offset:128
	s_waitcnt vmcnt(63) expcnt(7) lgkmcnt(15)
	s_barrier
	s_cbranch_scc0 .LBB0_506
